# speedup vs baseline: 1.1097x; 1.1097x over previous
_Z22k2_resolve_rank_gatherPKfS0_PKdS0_PKiPKyPKtS0_S4_Pf:
	s_load_dwordx16 s[4:19], s[0:1], 0x0
	s_load_dwordx4 s[20:23], s[0:1], 0x40
	v_and_b32_e32 v1, 0x3ff, v0
	s_lshr_b32 s24, s2, 6
	s_and_b32 s25, s2, 63
	s_lshl_b32 s26, s24, 9
	v_lshl_add_u32 v2, v1, 1, s26
	v_lshlrev_b32_e32 v3, 4, v2
	v_lshlrev_b32_e32 v24, 2, v2
	v_lshlrev_b32_e32 v25, 3, v2
	v_mov_b32_e32 v106, 0
	v_mov_b32_e32 v107, 0
	v_mov_b32_e32 v105, 0x1800
	v_lshlrev_b32_e32 v104, 3, v1
	s_movk_i32 s30, 0x641
	s_mov_b32 s32, 0xa0b5ed8d
	s_mov_b32 s33, 0x3ed0c6f7
	s_mov_b32 s34, 0xa0b5ed8d
	s_mov_b32 s35, 0xbed0c6f7
	s_mul_i32 s31, s26, 0x1904
	v_lshrrev_b32_e32 v29, 6, v1
	s_waitcnt lgkmcnt(0)
	global_load_dwordx4 v[4:7], v3, s[16:17]
	global_load_dwordx4 v[8:11], v3, s[16:17] offset:16
	global_load_dwordx2 v[12:13], v24, s[10:11]
	global_load_dwordx2 v[16:17], v24, s[12:13]
	global_load_dwordx4 v[20:23], v25, s[8:9]
	global_load_dwordx2 v[14:15], v24, s[18:19]
	global_load_dwordx2 v[18:19], v24, s[20:21]
	s_add_u32 s28, s4, s31
	s_addc_u32 s29, s5, 0
	v_readfirstlane_b32 s27, v29
	ds_write_b64 v105, v[106:107]
	ds_write_b64 v105, v[106:107] offset:8
	ds_write_b64 v105, v[106:107] offset:16
	ds_write_b64 v104, v[106:107] offset:8448
	s_mov_b64 s[36:37], 0
	s_mov_b64 s[38:39], 0
	s_mov_b64 s[40:41], 0
	s_mov_b64 s[42:43], 0
	s_mov_b64 s[44:45], 0
	v_lshlrev_b32_e32 v2, 4, v1
	s_waitcnt vmcnt(2)
	ds_write_b128 v2, v[20:23] offset:12544
	v_lshlrev_b32_e32 v3, 5, v1
	ds_write_b128 v3, v[4:7] offset:22784
	ds_write_b128 v3, v[8:11] offset:22800
	ds_write_b64 v104, v[16:17] offset:30976
	v_and_b32_e32 v26, 0xffff, v4
	v_and_b32_e32 v27, 0xffff, v8
	v_max_u32_e32 v28, v26, v27
	v_cvt_f64_f32_e32 v[92:93], v12
	v_cvt_f64_f32_e32 v[94:95], v13
	v_add_f64 v[92:93], v[92:93], -v[20:21]
	v_add_f64 v[94:95], v[94:95], -v[22:23]
	s_waitcnt vmcnt(0)
	ds_write_b64 v104, v[14:15] offset:33024
	v_cvt_f64_f32_e32 v[96:97], v14
	v_cvt_f64_f32_e32 v[98:99], v15
	v_add_f64 v[96:97], v[96:97], -v[20:21]
	v_add_f64 v[98:99], v[98:99], -v[22:23]
	s_waitcnt lgkmcnt(0)
	s_barrier
	v_cmp_lt_u32_e32 vcc, 0, v28
	s_cbranch_vccz .Lk2_l1_done
	v_cmp_lt_u32_e32 vcc, 0, v26
	s_and_saveexec_b64 s[46:47], vcc
	s_cbranch_execz .Lk2_l1_0_0
	v_lshrrev_b32_e32 v29, 16, v4
	v_mad_u32_u24 v30, v29, s30, v16
	v_mad_u32_u24 v31, v29, s30, v18
	v_lshlrev_b32_e32 v30, 2, v30
	v_lshlrev_b32_e32 v31, 2, v31
	v_lshlrev_b32_e32 v29, 3, v29
	global_load_dword v32, v30, s[28:29]
	global_load_dword v33, v31, s[28:29]
	ds_read_b64 v[34:35], v29 offset:12544

.Lk2_l2_done:
	s_mov_b64 s[52:53], 0
	s_mov_b64 s[50:51], s[36:37]
.Lk2_t15_loop0:
	s_cmp_eq_u64 s[50:51], 0
	s_cbranch_scc1 .Lk2_t15_done0
	s_ff1_i32_b64 s56, s[50:51]
	s_bitset0_b64 s[50:51], s56
	s_bitcmp1_b64 s[38:39], s56
	s_cbranch_scc1 .Lk2_t15_loop0
	s_lshl_b32 s57, s27, 6
	s_add_u32 s57, s57, s56
	s_lshl_b32 s57, s57, 1
	s_lshl_b32 s58, s57, 4
	v_readlane_b32 s59, v16, s56
	v_readlane_b32 s60, v92, s56
	v_readlane_b32 s61, v93, s56
	v_and_b32_e32 v32, 7, v1
	v_bfe_u32 v33, v1, 3, 3
	v_lshlrev_b32_e32 v34, 1, v32
	v_add_u32_e32 v34, s58, v34
	v_mov_b32_e32 v35, s58
	ds_read_u16 v36, v34 offset:22786
	ds_read_u16 v37, v35 offset:22784
	v_mov_b32_e32 v43, s59
	v_mov_b32_e32 v60, s60
	v_mov_b32_e32 v61, s61
	s_waitcnt lgkmcnt(0)
	v_cmp_lt_u32_e64 s[62:63], v32, v37
	s_nop 1
	v_cndmask_b32_e64 v36, 0, v36, s[62:63]
	v_lshlrev_b32_e32 v38, 4, v36
	v_lshl_add_u32 v39, v33, 1, v38
	ds_read_u16 v40, v39 offset:22786
	ds_read_u16 v41, v38 offset:22784
	v_lshlrev_b32_e32 v42, 3, v36
	ds_read_b64 v[44:45], v42 offset:12544
	v_mad_u32_u24 v46, v36, s30, v43
	v_lshlrev_b32_e32 v46, 2, v46
	global_load_dword v47, v46, s[28:29]
	s_waitcnt lgkmcnt(0)
	v_cmp_lt_u32_e64 s[64:65], v33, v41
	s_and_b64 s[64:65], s[64:65], s[62:63]
	v_cndmask_b32_e64 v40, 0, v40, s[64:65]
	v_lshlrev_b32_e32 v48, 3, v40
	ds_read_b64 v[50:51], v48 offset:12544
	v_mad_u32_u24 v49, v40, s30, v43
	v_lshlrev_b32_e32 v49, 2, v49
	global_load_dword v62, v49, s[28:29]
	s_waitcnt vmcnt(0) lgkmcnt(0)
	v_cvt_f64_f32_e32 v[54:55], v47
	v_cvt_f64_f32_e32 v[56:57], v62
	v_add_f64 v[54:55], v[54:55], -v[44:45]
	v_add_f64 v[56:57], v[56:57], -v[50:51]
	v_add_f64 v[58:59], v[54:55], -v[60:61]
	v_add_f64 v[56:57], v[56:57], -v[54:55]
	v_cmp_lt_f64_e64 s[66:67], s[32:33], v[58:59]
	v_cmp_le_f64_e64 s[68:69], s[34:35], v[56:57]
	s_and_b64 s[66:67], s[66:67], s[62:63]
	s_and_b32 s66, s66, 0xff
	s_and_b64 s[68:69], s[68:69], s[64:65]
	s_or_b32 s68, s68, s69
	s_lshr_b32 s69, s68, 16
	s_or_b32 s68, s68, s69
	s_lshr_b32 s69, s68, 8
	s_or_b32 s68, s68, s69
	s_andn2_b32 s66, s66, s68
	s_and_b32 s66, s66, 0xff
	s_cmp_eq_u32 s66, 0
	s_cbranch_scc1 .Lk2_t15_loop0
	s_bitset1_b64 s[52:53], s56
	s_bitset0_b64 s[36:37], s56
	s_branch .Lk2_t15_loop0
.Lk2_t15_done0:
	s_mov_b64 s[54:55], 0
	s_mov_b64 s[50:51], s[40:41]
.Lk2_t15_loop1:
	s_cmp_eq_u64 s[50:51], 0
	s_cbranch_scc1 .Lk2_t15_done1
	s_ff1_i32_b64 s56, s[50:51]
	s_bitset0_b64 s[50:51], s56
	s_bitcmp1_b64 s[42:43], s56
	s_cbranch_scc1 .Lk2_t15_loop1
	s_lshl_b32 s57, s27, 6
	s_add_u32 s57, s57, s56
	s_lshl_b32 s57, s57, 1
	s_add_u32 s57, s57, 1
	s_lshl_b32 s58, s57, 4
	v_readlane_b32 s59, v17, s56
	v_readlane_b32 s60, v94, s56
	v_readlane_b32 s61, v95, s56
	v_and_b32_e32 v32, 7, v1
	v_bfe_u32 v33, v1, 3, 3
	v_lshlrev_b32_e32 v34, 1, v32
	v_add_u32_e32 v34, s58, v34
	v_mov_b32_e32 v35, s58
	ds_read_u16 v36, v34 offset:22786
	ds_read_u16 v37, v35 offset:22784
	v_mov_b32_e32 v43, s59
	v_mov_b32_e32 v60, s60
	v_mov_b32_e32 v61, s61
	s_waitcnt lgkmcnt(0)
	v_cmp_lt_u32_e64 s[62:63], v32, v37
	s_nop 1
	v_cndmask_b32_e64 v36, 0, v36, s[62:63]
	v_lshlrev_b32_e32 v38, 4, v36
	v_lshl_add_u32 v39, v33, 1, v38
	ds_read_u16 v40, v39 offset:22786
	ds_read_u16 v41, v38 offset:22784
	v_lshlrev_b32_e32 v42, 3, v36
	ds_read_b64 v[44:45], v42 offset:12544
	v_mad_u32_u24 v46, v36, s30, v43
	v_lshlrev_b32_e32 v46, 2, v46
	global_load_dword v47, v46, s[28:29]
	s_waitcnt lgkmcnt(0)
	v_cmp_lt_u32_e64 s[64:65], v33, v41
	s_and_b64 s[64:65], s[64:65], s[62:63]
	v_cndmask_b32_e64 v40, 0, v40, s[64:65]
	v_lshlrev_b32_e32 v48, 3, v40
	ds_read_b64 v[50:51], v48 offset:12544
	v_mad_u32_u24 v49, v40, s30, v43
	v_lshlrev_b32_e32 v49, 2, v49
	global_load_dword v62, v49, s[28:29]
	s_waitcnt vmcnt(0) lgkmcnt(0)
	v_cvt_f64_f32_e32 v[54:55], v47
	v_cvt_f64_f32_e32 v[56:57], v62
	v_add_f64 v[54:55], v[54:55], -v[44:45]
	v_add_f64 v[56:57], v[56:57], -v[50:51]
	v_add_f64 v[58:59], v[54:55], -v[60:61]
	v_add_f64 v[56:57], v[56:57], -v[54:55]
	v_cmp_lt_f64_e64 s[66:67], s[32:33], v[58:59]
	v_cmp_le_f64_e64 s[68:69], s[34:35], v[56:57]
	s_and_b64 s[66:67], s[66:67], s[62:63]
	s_and_b32 s66, s66, 0xff
	s_and_b64 s[68:69], s[68:69], s[64:65]
	s_or_b32 s68, s68, s69
	s_lshr_b32 s69, s68, 16
	s_or_b32 s68, s68, s69
	s_lshr_b32 s69, s68, 8
	s_or_b32 s68, s68, s69
	s_andn2_b32 s66, s66, s68
	s_and_b32 s66, s66, 0xff
	s_cmp_eq_u32 s66, 0
	s_cbranch_scc1 .Lk2_t15_loop1
	s_bitset1_b64 s[54:55], s56
	s_bitset0_b64 s[40:41], s56
	s_branch .Lk2_t15_loop1
.Lk2_t15_done1:
	v_cndmask_b32_e64 v92, v92, v96, s[52:53]
	v_cndmask_b32_e64 v93, v93, v97, s[52:53]
	v_cndmask_b32_e64 v12, v12, v14, s[52:53]
	v_cndmask_b32_e64 v94, v94, v98, s[54:55]
	v_cndmask_b32_e64 v95, v95, v99, s[54:55]
	v_cndmask_b32_e64 v13, v13, v15, s[54:55]
	ds_write_b128 v2, v[92:95] offset:0
	ds_write_b64 v104, v[12:13] offset:4096
	v_cmp_lt_u32_e32 vcc, 7, v28
	s_or_b64 s[48:49], vcc, s[44:45]
	s_cmp_eq_u64 s[48:49], 0
	s_cbranch_scc1 .Lk2_nofb
	v_mov_b32_e32 v30, 1
	ds_write_b32 v105, v30 offset:8

.Lk2_rank:
	ds_read_b64 v[64:65], v29 offset:0
	ds_read_b64 v[32:33], v31 offset:0
	ds_read_b64 v[34:35], v31 offset:256
	ds_read_b64 v[36:37], v31 offset:512
	ds_read_b64 v[38:39], v31 offset:768
	ds_read_b64 v[40:41], v31 offset:1024
	ds_read_b64 v[42:43], v31 offset:1280
	ds_read_b64 v[44:45], v31 offset:1536
	ds_read_b64 v[46:47], v31 offset:1792
	ds_read_b64 v[48:49], v31 offset:2048
	ds_read_b64 v[50:51], v31 offset:2304
	ds_read_b64 v[52:53], v31 offset:2560
	ds_read_b64 v[54:55], v31 offset:2816
	ds_read_b64 v[56:57], v31 offset:3072
	v_mov_b32_e32 v66, 0
	v_mov_b32_e32 v67, 0
	s_waitcnt lgkmcnt(12)
	ds_read_b64 v[58:59], v31 offset:3328
	v_add_f64 v[88:89], v[32:33], -v[64:65]
	v_cmp_lt_f64_e32 vcc, s[32:33], v[88:89]
	v_cmp_ge_f64_e64 s[48:49], s[32:33], |v[88:89]|
	s_nop 0
	v_addc_co_u32_e32 v66, vcc, 0, v66, vcc
	v_addc_co_u32_e64 v67, s[50:51], 0, v67, s[48:49]
	s_waitcnt lgkmcnt(12)
	ds_read_b64 v[60:61], v31 offset:3584
	v_add_f64 v[88:89], v[34:35], -v[64:65]
	v_cmp_lt_f64_e32 vcc, s[32:33], v[88:89]
	v_cmp_ge_f64_e64 s[48:49], s[32:33], |v[88:89]|
	s_nop 0
	v_addc_co_u32_e32 v66, vcc, 0, v66, vcc
	v_addc_co_u32_e64 v67, s[50:51], 0, v67, s[48:49]
	s_waitcnt lgkmcnt(12)
	ds_read_b64 v[62:63], v31 offset:3840
	v_add_f64 v[88:89], v[36:37], -v[64:65]
	v_cmp_lt_f64_e32 vcc, s[32:33], v[88:89]
	v_cmp_ge_f64_e64 s[48:49], s[32:33], |v[88:89]|
	s_nop 0
	v_addc_co_u32_e32 v66, vcc, 0, v66, vcc
	v_addc_co_u32_e64 v67, s[50:51], 0, v67, s[48:49]
	s_waitcnt lgkmcnt(12)
	v_add_f64 v[88:89], v[38:39], -v[64:65]
	v_cmp_lt_f64_e32 vcc, s[32:33], v[88:89]
	v_cmp_ge_f64_e64 s[48:49], s[32:33], |v[88:89]|
	s_nop 0
	v_addc_co_u32_e32 v66, vcc, 0, v66, vcc
	v_addc_co_u32_e64 v67, s[50:51], 0, v67, s[48:49]
	s_waitcnt lgkmcnt(11)
	v_add_f64 v[88:89], v[40:41], -v[64:65]
	v_cmp_lt_f64_e32 vcc, s[32:33], v[88:89]
	v_cmp_ge_f64_e64 s[48:49], s[32:33], |v[88:89]|
	s_nop 0
	v_addc_co_u32_e32 v66, vcc, 0, v66, vcc
	v_addc_co_u32_e64 v67, s[50:51], 0, v67, s[48:49]
	s_waitcnt lgkmcnt(10)
	v_add_f64 v[88:89], v[42:43], -v[64:65]
	v_cmp_lt_f64_e32 vcc, s[32:33], v[88:89]
	v_cmp_ge_f64_e64 s[48:49], s[32:33], |v[88:89]|
	s_nop 0
	v_addc_co_u32_e32 v66, vcc, 0, v66, vcc
	v_addc_co_u32_e64 v67, s[50:51], 0, v67, s[48:49]
	s_waitcnt lgkmcnt(9)
	v_add_f64 v[88:89], v[44:45], -v[64:65]
	v_cmp_lt_f64_e32 vcc, s[32:33], v[88:89]
	v_cmp_ge_f64_e64 s[48:49], s[32:33], |v[88:89]|
	s_nop 0
	v_addc_co_u32_e32 v66, vcc, 0, v66, vcc
	v_addc_co_u32_e64 v67, s[50:51], 0, v67, s[48:49]
	s_waitcnt lgkmcnt(8)
	v_add_f64 v[88:89], v[46:47], -v[64:65]
	v_cmp_lt_f64_e32 vcc, s[32:33], v[88:89]
	v_cmp_ge_f64_e64 s[48:49], s[32:33], |v[88:89]|
	s_nop 0
	v_addc_co_u32_e32 v66, vcc, 0, v66, vcc
	v_addc_co_u32_e64 v67, s[50:51], 0, v67, s[48:49]
	s_waitcnt lgkmcnt(7)
	v_add_f64 v[88:89], v[48:49], -v[64:65]
	v_cmp_lt_f64_e32 vcc, s[32:33], v[88:89]
	v_cmp_ge_f64_e64 s[48:49], s[32:33], |v[88:89]|
	s_nop 0
	v_addc_co_u32_e32 v66, vcc, 0, v66, vcc
	v_addc_co_u32_e64 v67, s[50:51], 0, v67, s[48:49]
	s_waitcnt lgkmcnt(6)
	v_add_f64 v[88:89], v[50:51], -v[64:65]
	v_cmp_lt_f64_e32 vcc, s[32:33], v[88:89]
	v_cmp_ge_f64_e64 s[48:49], s[32:33], |v[88:89]|
	s_nop 0
	v_addc_co_u32_e32 v66, vcc, 0, v66, vcc
	v_addc_co_u32_e64 v67, s[50:51], 0, v67, s[48:49]
	s_waitcnt lgkmcnt(5)
	v_add_f64 v[88:89], v[52:53], -v[64:65]
	v_cmp_lt_f64_e32 vcc, s[32:33], v[88:89]
	v_cmp_ge_f64_e64 s[48:49], s[32:33], |v[88:89]|
	s_nop 0
	v_addc_co_u32_e32 v66, vcc, 0, v66, vcc
	v_addc_co_u32_e64 v67, s[50:51], 0, v67, s[48:49]
	s_waitcnt lgkmcnt(4)
	v_add_f64 v[88:89], v[54:55], -v[64:65]
	v_cmp_lt_f64_e32 vcc, s[32:33], v[88:89]
	v_cmp_ge_f64_e64 s[48:49], s[32:33], |v[88:89]|
	s_nop 0
	v_addc_co_u32_e32 v66, vcc, 0, v66, vcc
	v_addc_co_u32_e64 v67, s[50:51], 0, v67, s[48:49]
	s_waitcnt lgkmcnt(3)
	v_add_f64 v[88:89], v[56:57], -v[64:65]
	v_cmp_lt_f64_e32 vcc, s[32:33], v[88:89]
	v_cmp_ge_f64_e64 s[48:49], s[32:33], |v[88:89]|
	s_nop 0
	v_addc_co_u32_e32 v66, vcc, 0, v66, vcc
	v_addc_co_u32_e64 v67, s[50:51], 0, v67, s[48:49]
	s_waitcnt lgkmcnt(2)
	v_add_f64 v[88:89], v[58:59], -v[64:65]
	v_cmp_lt_f64_e32 vcc, s[32:33], v[88:89]
	v_cmp_ge_f64_e64 s[48:49], s[32:33], |v[88:89]|
	s_nop 0
	v_addc_co_u32_e32 v66, vcc, 0, v66, vcc
	v_addc_co_u32_e64 v67, s[50:51], 0, v67, s[48:49]
	s_waitcnt lgkmcnt(1)
	v_add_f64 v[88:89], v[60:61], -v[64:65]
	v_cmp_lt_f64_e32 vcc, s[32:33], v[88:89]
	v_cmp_ge_f64_e64 s[48:49], s[32:33], |v[88:89]|
	s_nop 0
	v_addc_co_u32_e32 v66, vcc, 0, v66, vcc
	v_addc_co_u32_e64 v67, s[50:51], 0, v67, s[48:49]
	s_waitcnt lgkmcnt(0)
	v_add_f64 v[88:89], v[62:63], -v[64:65]
	v_cmp_lt_f64_e32 vcc, s[32:33], v[88:89]
	v_cmp_ge_f64_e64 s[48:49], s[32:33], |v[88:89]|
	s_nop 0
	v_addc_co_u32_e32 v66, vcc, 0, v66, vcc
	v_addc_co_u32_e64 v67, s[50:51], 0, v67, s[48:49]
	v_lshl_or_b32 v68, v67, 16, v66
	s_nop 1
	v_add_u32_dpp v68, v68, v68 quad_perm:[1,0,3,2] row_mask:0xf bank_mask:0xf
	s_nop 1
	v_add_u32_dpp v68, v68, v68 quad_perm:[2,3,0,1] row_mask:0xf bank_mask:0xf
	s_nop 1
	v_add_u32_dpp v68, v68, v68 row_half_mirror row_mask:0xf bank_mask:0xf
	s_nop 1
	v_add_u32_dpp v68, v68, v68 row_mirror row_mask:0xf bank_mask:0xf
	s_nop 1
	v_add_u32_dpp v68, v68, v68 row_bcast:15 row_mask:0xa bank_mask:0xf
	s_nop 1
	v_readlane_b32 s52, v68, 31
	v_readlane_b32 s53, v68, 63
	v_and_b32_e32 v69, 63, v1
	v_lshlrev_b32_e32 v69, 4, v69
	v_add_u32_e32 v70, 0x1000, v69
	s_and_b32 s54, s52, 0xffff
	s_lshr_b32 s55, s52, 16
	s_and_b32 s56, s53, 0xffff
	s_lshr_b32 s57, s53, 16
	s_cmp_gt_u32 s55, 1
	s_cselect_b32 s58, 1, 0
	s_cmp_lt_u32 s54, 0x64
	s_cselect_b32 s59, 1, 0
	s_and_b32 s58, s58, s59
	s_cmp_gt_u32 s57, 1
	s_cselect_b32 s60, 1, 0
	s_cmp_lt_u32 s56, 0x64
	s_cselect_b32 s61, 1, 0
	s_and_b32 s60, s60, s61
	s_or_b32 s61, s58, s60
	s_lshl_b32 s62, s25, 3
	s_lshl_b32 s63, s27, 1
	s_add_u32 s62, s62, s63
	s_add_u32 s62, s62, s26
	s_lshl_b32 s62, s62, 13
	s_add_u32 s64, s6, s62
	s_addc_u32 s65, s7, 0
	s_add_u32 s66, s64, 0x2000
	s_addc_u32 s67, s65, 0
	s_cmp_lt_u32 s54, 0x64
	s_cbranch_scc0 .Lk2_ga_skip
	global_load_dwordx4 v[32:35], v69, s[64:65] offset:0 nt
	global_load_dwordx4 v[36:39], v69, s[64:65] offset:1024 nt
	global_load_dwordx4 v[40:43], v69, s[64:65] offset:2048 nt
	global_load_dwordx4 v[44:47], v69, s[64:65] offset:3072 nt
	global_load_dwordx4 v[48:51], v70, s[64:65] offset:0 nt
	global_load_dwordx4 v[52:55], v70, s[64:65] offset:1024 nt
	global_load_dwordx4 v[56:59], v70, s[64:65] offset:2048 nt
	global_load_dwordx4 v[60:63], v70, s[64:65] offset:3072 nt

.Lk2_gb_skip:
	s_cmp_lg_u32 s61, 0
	s_cbranch_scc1 .Lk2_needref

.Lk2_nr_loop:
	ds_read_b64 v[116:117], v29 offset:0
	s_waitcnt lgkmcnt(0)
	v_add_f64 v[116:117], v[116:117], -v[64:65]
	v_cmp_ge_f64_e64 s[50:51], s[32:33], |v[116:117]|
	s_and_saveexec_b64 s[46:47], s[50:51]
	ds_write_b32 v30, v31 offset:8448
	s_mov_b64 exec, s[46:47]
	v_add_u32_e32 v29, 0x100, v29
	v_add_u32_e32 v30, 0x80, v30
	s_sub_u32 s3, s3, 1
	s_cmp_lg_u32 s3, 0
	s_cbranch_scc1 .Lk2_nr_loop
	s_mov_b64 exec, -1
	ds_write_b32 v105, v31 offset:16
	s_waitcnt lgkmcnt(0)
	s_branch .Lk2_b3

.Lk2_rf_loop:
	s_cmp_lt_u32 s99, s98
	s_cbranch_scc0 .Lk2_rf_done
	v_mov_b32_e32 v29, s99
	v_lshlrev_b32_e32 v29, 2, v29
	ds_read_b32 v30, v29 offset:6400
	s_waitcnt lgkmcnt(0)
	v_readfirstlane_b32 s48, v30
	s_mul_i32 s3, s48, 0x1904
	s_add_u32 s50, s28, s3
	s_addc_u32 s51, s29, 0
	s_load_dword s49, s[50:51], 0x1900
	global_load_dword v4, v3, s[50:51] offset:0
	global_load_dword v5, v3, s[50:51] offset:256
	global_load_dword v6, v3, s[50:51] offset:512
	global_load_dword v7, v3, s[50:51] offset:768
	global_load_dword v8, v3, s[50:51] offset:1024
	global_load_dword v9, v3, s[50:51] offset:1280
	global_load_dword v10, v3, s[50:51] offset:1536
	global_load_dword v11, v3, s[50:51] offset:1792
	global_load_dword v12, v3, s[50:51] offset:2048
	global_load_dword v13, v3, s[50:51] offset:2304
	global_load_dword v14, v3, s[50:51] offset:2560
	global_load_dword v15, v3, s[50:51] offset:2816
	global_load_dword v16, v3, s[50:51] offset:3072
	global_load_dword v17, v3, s[50:51] offset:3328
	global_load_dword v18, v3, s[50:51] offset:3584
	global_load_dword v19, v3, s[50:51] offset:3840
	global_load_dword v20, v114, s[50:51] offset:0
	global_load_dword v21, v114, s[50:51] offset:256
	global_load_dword v22, v114, s[50:51] offset:512
	global_load_dword v23, v114, s[50:51] offset:768
	global_load_dword v24, v114, s[50:51] offset:1024
	global_load_dword v25, v114, s[50:51] offset:1280
	global_load_dword v26, v114, s[50:51] offset:1536
	global_load_dword v27, v114, s[50:51] offset:1792
	global_load_dword v28, v114, s[50:51] offset:2048
	s_waitcnt vmcnt(0) lgkmcnt(0)
	ds_write_b32 v115, v4 offset:12544
	ds_write_b32 v115, v5 offset:12800
	ds_write_b32 v115, v6 offset:13056
	ds_write_b32 v115, v7 offset:13312
	ds_write_b32 v115, v8 offset:13568
	ds_write_b32 v115, v9 offset:13824
	ds_write_b32 v115, v10 offset:14080
	ds_write_b32 v115, v11 offset:14336
	ds_write_b32 v115, v12 offset:14592
	ds_write_b32 v115, v13 offset:14848
	ds_write_b32 v115, v14 offset:15104
	ds_write_b32 v115, v15 offset:15360
	ds_write_b32 v115, v16 offset:15616
	ds_write_b32 v115, v17 offset:15872
	ds_write_b32 v115, v18 offset:16128
	ds_write_b32 v115, v19 offset:16384
	ds_write_b32 v115, v20 offset:16640
	ds_write_b32 v115, v21 offset:16896
	ds_write_b32 v115, v22 offset:17152
	ds_write_b32 v115, v23 offset:17408
	ds_write_b32 v115, v24 offset:17664
	ds_write_b32 v115, v25 offset:17920
	ds_write_b32 v115, v26 offset:18176
	ds_write_b32 v115, v27 offset:18432
	ds_write_b32 v115, v28 offset:18688
	v_max3_f32 v116, v4, v5, v6
	v_max3_f32 v116, v116, v7, v8
	v_max3_f32 v116, v116, v9, v10
	v_max3_f32 v116, v116, v11, v12
	v_max3_f32 v116, v116, v13, v14
	v_max3_f32 v116, v116, v15, v16
	v_max3_f32 v116, v116, v17, v18
	v_max3_f32 v116, v116, v19, v20
	v_max3_f32 v116, v116, v21, v22
	v_max3_f32 v116, v116, v23, v24
	v_max3_f32 v116, v116, v25, v26
	v_max3_f32 v116, v116, v27, v28
	v_max_f32_e32 v116, s49, v116
	s_nop 1
	v_max_f32_dpp v116, v116, v116 quad_perm:[1,0,3,2] row_mask:0xf bank_mask:0xf
	s_nop 1
	v_max_f32_dpp v116, v116, v116 quad_perm:[2,3,0,1] row_mask:0xf bank_mask:0xf
	s_nop 1
	v_max_f32_dpp v116, v116, v116 row_half_mirror row_mask:0xf bank_mask:0xf
	s_nop 1
	v_max_f32_dpp v116, v116, v116 row_mirror row_mask:0xf bank_mask:0xf
	s_nop 1
	v_max_f32_dpp v116, v116, v116 row_bcast:15 row_mask:0xa bank_mask:0xf
	s_nop 1
	v_max_f32_dpp v116, v116, v116 row_bcast:31 row_mask:0xc bank_mask:0xf
	s_nop 1
	v_readlane_b32 s31, v116, 63
	s_nop 1
	v_cvt_f64_f32_e32 v[118:119], s31
	v_mov_b32_e32 v110, 0
	v_mov_b32_e32 v111, 0
	v_mov_b32_e32 v66, 0
	v_mov_b32_e32 v67, 0
	v_mov_b32_e32 v29, v115
	s_waitcnt lgkmcnt(0)
	ds_read_b32 v30, v29 offset:12544
	ds_read_b32 v31, v29 offset:15616
	s_mov_b32 s3, 12
.Lk2_rf_exp:
	s_waitcnt lgkmcnt(0)
	v_cvt_f64_f32_e32 v[120:121], v30
	v_cvt_f64_f32_e32 v[116:117], v31
	v_add_u32_e32 v29, 0x100, v29
	s_cmp_eq_u32 s3, 1
	s_cbranch_scc1 .Lk2_rf_lastpf
	ds_read_b32 v30, v29 offset:12544
	ds_read_b32 v31, v29 offset:15616
	s_branch .Lk2_rf_nopf
.Lk2_rf_lastpf:
	ds_read_b32 v30, v29 offset:15616
.Lk2_rf_nopf:
	v_add_f64 v[120:121], v[120:121], -v[118:119]
	v_add_f64 v[116:117], v[116:117], -v[118:119]
	v_mul_f64 v[122:123], v[120:121], s[74:75]
	v_mul_f64 v[112:113], v[116:117], s[74:75]
	v_rndne_f64_e32 v[122:123], v[122:123]
	v_rndne_f64_e32 v[112:113], v[112:113]
	v_fma_f64 v[120:121], v[122:123], s[76:77], v[120:121]
	v_fma_f64 v[116:117], v[112:113], s[76:77], v[116:117]
	v_fma_f64 v[120:121], v[122:123], s[78:79], v[120:121]
	v_fma_f64 v[116:117], v[112:113], s[78:79], v[116:117]
	v_fma_f64 v[124:125], v[108:109], v[120:121], s[80:81]
	v_fma_f64 v[64:65], v[108:109], v[116:117], s[80:81]
	v_fma_f64 v[124:125], v[124:125], v[120:121], s[82:83]
	v_fma_f64 v[64:65], v[64:65], v[116:117], s[82:83]
	v_fma_f64 v[124:125], v[124:125], v[120:121], s[84:85]
	v_fma_f64 v[64:65], v[64:65], v[116:117], s[84:85]
	v_fma_f64 v[124:125], v[124:125], v[120:121], s[86:87]
	v_fma_f64 v[64:65], v[64:65], v[116:117], s[86:87]
	v_fma_f64 v[124:125], v[124:125], v[120:121], s[88:89]
	v_fma_f64 v[64:65], v[64:65], v[116:117], s[88:89]
	v_fma_f64 v[124:125], v[124:125], v[120:121], s[90:91]
	v_fma_f64 v[64:65], v[64:65], v[116:117], s[90:91]
	v_fma_f64 v[124:125], v[124:125], v[120:121], s[92:93]
	v_fma_f64 v[64:65], v[64:65], v[116:117], s[92:93]
	v_fma_f64 v[124:125], v[124:125], v[120:121], s[94:95]
	v_fma_f64 v[64:65], v[64:65], v[116:117], s[94:95]
	v_fma_f64 v[124:125], v[124:125], v[120:121], 0.5
	v_fma_f64 v[64:65], v[64:65], v[116:117], 0.5
	v_fma_f64 v[124:125], v[124:125], v[120:121], 1.0
	v_fma_f64 v[64:65], v[64:65], v[116:117], 1.0
	v_fma_f64 v[124:125], v[124:125], v[120:121], 1.0
	v_fma_f64 v[64:65], v[64:65], v[116:117], 1.0
	v_cvt_i32_f64_e32 v126, v[122:123]
	v_cvt_i32_f64_e32 v68, v[112:113]
	v_ldexp_f64 v[124:125], v[124:125], v126
	v_ldexp_f64 v[64:65], v[64:65], v68
	v_add_f64 v[110:111], v[110:111], v[124:125]
	v_add_f64 v[66:67], v[66:67], v[64:65]
	s_sub_u32 s3, s3, 1
	s_cmp_lg_u32 s3, 0
	s_cbranch_scc1 .Lk2_rf_exp
	s_waitcnt lgkmcnt(0)
	v_cvt_f64_f32_e32 v[120:121], v30
	v_add_f64 v[120:121], v[120:121], -v[118:119]
	v_mul_f64 v[122:123], v[120:121], s[74:75]
	v_rndne_f64_e32 v[122:123], v[122:123]
	v_fma_f64 v[120:121], v[122:123], s[76:77], v[120:121]
	v_fma_f64 v[120:121], v[122:123], s[78:79], v[120:121]
	v_fma_f64 v[124:125], v[108:109], v[120:121], s[80:81]
	v_fma_f64 v[124:125], v[124:125], v[120:121], s[82:83]
	v_fma_f64 v[124:125], v[124:125], v[120:121], s[84:85]
	v_fma_f64 v[124:125], v[124:125], v[120:121], s[86:87]
	v_fma_f64 v[124:125], v[124:125], v[120:121], s[88:89]
	v_fma_f64 v[124:125], v[124:125], v[120:121], s[90:91]
	v_fma_f64 v[124:125], v[124:125], v[120:121], s[92:93]
	v_fma_f64 v[124:125], v[124:125], v[120:121], s[94:95]
	v_fma_f64 v[124:125], v[124:125], v[120:121], 0.5
	v_fma_f64 v[124:125], v[124:125], v[120:121], 1.0
	v_fma_f64 v[124:125], v[124:125], v[120:121], 1.0
	v_cvt_i32_f64_e32 v126, v[122:123]
	v_ldexp_f64 v[124:125], v[124:125], v126
	v_add_f64 v[110:111], v[110:111], v[124:125]
	v_add_f64 v[110:111], v[110:111], v[66:67]
	s_nop 1
	v_mov_b32_dpp v126, v110 quad_perm:[1,0,3,2] row_mask:0xf bank_mask:0xf
	v_mov_b32_dpp v127, v111 quad_perm:[1,0,3,2] row_mask:0xf bank_mask:0xf
	v_add_f64 v[110:111], v[110:111], v[126:127]
	s_nop 1
	v_mov_b32_dpp v126, v110 quad_perm:[2,3,0,1] row_mask:0xf bank_mask:0xf
	v_mov_b32_dpp v127, v111 quad_perm:[2,3,0,1] row_mask:0xf bank_mask:0xf
	v_add_f64 v[110:111], v[110:111], v[126:127]
	s_nop 1
	v_mov_b32_dpp v126, v110 row_half_mirror row_mask:0xf bank_mask:0xf
	v_mov_b32_dpp v127, v111 row_half_mirror row_mask:0xf bank_mask:0xf
	v_add_f64 v[110:111], v[110:111], v[126:127]
	s_nop 1
	v_mov_b32_dpp v126, v110 row_mirror row_mask:0xf bank_mask:0xf
	v_mov_b32_dpp v127, v111 row_mirror row_mask:0xf bank_mask:0xf
	v_add_f64 v[110:111], v[110:111], v[126:127]
	s_nop 1
	v_readlane_b32 s52, v110, 15
	v_readlane_b32 s53, v111, 15
	v_readlane_b32 s96, v110, 31
	v_readlane_b32 s97, v111, 31
	v_readlane_b32 s50, v110, 47
	v_readlane_b32 s51, v111, 47
	v_readlane_b32 s46, v110, 63
	v_readlane_b32 s47, v111, 63
	v_add_f64 v[110:111], s[52:53], 0
	v_add_f64 v[110:111], v[110:111], s[96:97]
	v_add_f64 v[110:111], v[110:111], s[50:51]
	v_add_f64 v[110:111], v[110:111], s[46:47]
	v_cvt_f64_f32_e32 v[120:121], s49
	v_add_f64 v[120:121], v[120:121], -v[118:119]
	v_mul_f64 v[122:123], v[120:121], s[74:75]
	v_rndne_f64_e32 v[122:123], v[122:123]
	v_fma_f64 v[120:121], v[122:123], s[76:77], v[120:121]
	v_fma_f64 v[120:121], v[122:123], s[78:79], v[120:121]
	v_fma_f64 v[124:125], v[108:109], v[120:121], s[80:81]
	v_fma_f64 v[124:125], v[124:125], v[120:121], s[82:83]
	v_fma_f64 v[124:125], v[124:125], v[120:121], s[84:85]
	v_fma_f64 v[124:125], v[124:125], v[120:121], s[86:87]
	v_fma_f64 v[124:125], v[124:125], v[120:121], s[88:89]
	v_fma_f64 v[124:125], v[124:125], v[120:121], s[90:91]
	v_fma_f64 v[124:125], v[124:125], v[120:121], s[92:93]
	v_fma_f64 v[124:125], v[124:125], v[120:121], s[94:95]
	v_fma_f64 v[124:125], v[124:125], v[120:121], 0.5
	v_fma_f64 v[124:125], v[124:125], v[120:121], 1.0
	v_fma_f64 v[124:125], v[124:125], v[120:121], 1.0
	v_cvt_i32_f64_e32 v126, v[122:123]
	v_ldexp_f64 v[124:125], v[124:125], v126
	v_add_f64 v[110:111], v[110:111], v[124:125]
	v_cvt_f32_f64_e32 v126, v[110:111]
	v_log_f32_e32 v126, v126
	s_nop 0
	v_mul_f32_e32 v126, 0x3f317218, v126
	v_cvt_f64_f32_e32 v[112:113], v126
	s_mov_b32 s3, 2

.Lk2_rc_loop:
	ds_read_b64 v[116:117], v30 offset:0
	s_waitcnt lgkmcnt(0)
	v_cmp_gt_f64_e32 vcc, v[116:117], v[64:65]
	v_cmp_eq_f64_e64 s[48:49], v[116:117], v[64:65]
	v_cmp_lt_u32_e64 s[50:51], v31, v29
	s_and_b64 s[48:49], s[48:49], s[50:51]
	s_or_b64 s[48:49], s[48:49], vcc
	v_addc_co_u32_e64 v66, s[50:51], 0, v66, s[48:49]
	v_add_u32_e32 v30, 0x100, v30
	v_add_u32_e32 v31, 32, v31
	s_sub_u32 s3, s3, 1
	s_cmp_lg_u32 s3, 0
	s_cbranch_scc1 .Lk2_rc_loop
	s_nop 1
	v_add_u32_dpp v66, v66, v66 quad_perm:[1,0,3,2] row_mask:0xf bank_mask:0xf
	s_nop 1
	v_add_u32_dpp v66, v66, v66 quad_perm:[2,3,0,1] row_mask:0xf bank_mask:0xf
	s_nop 1
	v_add_u32_dpp v66, v66, v66 row_half_mirror row_mask:0xf bank_mask:0xf
	s_nop 1
	v_add_u32_dpp v66, v66, v66 row_mirror row_mask:0xf bank_mask:0xf
	s_nop 1
	v_add_u32_dpp v66, v66, v66 row_bcast:15 row_mask:0xa bank_mask:0xf
	s_nop 1
	v_readlane_b32 s52, v66, 31
	v_readlane_b32 s53, v66, 63
	s_cmp_lg_u32 s58, 0
	s_cselect_b32 s54, s52, s54
	s_cmp_lg_u32 s60, 0
	s_cselect_b32 s56, s53, s56
	s_waitcnt vmcnt(0)
	s_branch .Lk2_dst_stores

.Lk2_h_loop:
	v_mov_b32_e32 v29, s75
	v_lshlrev_b32_e32 v29, 2, v29
	ds_read_b32 v30, v29 offset:10496
	s_waitcnt lgkmcnt(0)
	v_readfirstlane_b32 s76, v30
	s_and_b32 s77, s76, 0xffff
	s_lshr_b32 s78, s76, 16
	v_mov_b32_e32 v29, s77
	v_lshlrev_b32_e32 v29, 2, v29
	ds_read_b32 v30, v29 offset:30976
	ds_read_b32 v31, v29 offset:33024
	v_lshlrev_b32_e32 v88, 1, v1
	s_waitcnt lgkmcnt(0)
	v_readfirstlane_b32 s80, v30
	v_readfirstlane_b32 s81, v31
	v_mov_b32_e32 v29, s80
	v_mad_u32_u24 v30, v88, s30, v29
	v_add_u32_e32 v31, 0x641, v30
	v_lshlrev_b32_e32 v30, 2, v30
	v_lshlrev_b32_e32 v31, 2, v31
	global_load_dword v89, v30, s[28:29]
	global_load_dword v90, v31, s[28:29]
	v_cmp_eq_u32_e32 vcc, 0, v26
	v_cmp_eq_u32_e64 s[48:49], 0, v27
	s_nop 1
	v_cndmask_b32_e64 v112, 0, 1, vcc
	v_cndmask_b32_e64 v113, 0, 1, s[48:49]
	ds_write_b64 v104, v[112:113] offset:16640
	s_waitcnt vmcnt(0)
	v_cvt_f64_f32_e32 v[92:93], v89
	v_cvt_f64_f32_e32 v[94:95], v90
	v_add_f64 v[92:93], v[92:93], -v[20:21]
	v_add_f64 v[94:95], v[94:95], -v[22:23]
	ds_write_b128 v2, v[92:95] offset:18688
	s_waitcnt lgkmcnt(0)
	s_barrier
